# v085 + P0 rmsnorm loop: next row prefetched one iteration ahead, b_forget load hoisted, log-f store deferred past the top wait
# speedup vs baseline: 1.0039x; 1.0039x over previous
.LBB0_22:
	s_or_b64 exec, exec, s[0:1]
	s_ashr_i32 s0, s28, 31
	s_lshr_b32 s0, s0, 29
	s_add_i32 s0, s28, s0
	s_lshr_b32 s0, s0, 3
	s_lshl_b32 s1, s28, 8
	s_mulk_i32 s0, 0xf808
	s_ashr_i32 s30, s29, 6
	s_add_i32 s0, s0, s1
	v_and_b32_e32 v1, 63, v1
	s_add_i32 s18, s0, s30
	s_cmpk_lt_i32 s18, 0x2000
	v_lshlrev_b32_e32 v66, 2, v1
	s_waitcnt lgkmcnt(0)
	s_barrier
	s_cbranch_scc0 .LBB0_27
	v_readlane_b32 s48, v255, 21
	v_lshlrev_b32_e32 v34, 5, v1
	v_mov_b32_e32 v35, 0
	v_readlane_b32 s60, v255, 33
	v_readlane_b32 s61, v255, 34
	s_mov_b64 s[0:1], 0x1000
	v_readlane_b32 s40, v255, 1
	v_lshl_add_u64 v[2:3], s[60:61], 0, v[34:35]
	v_lshl_add_u64 v[38:39], v[2:3], 0, s[0:1]
	v_add_co_u32_e32 v36, vcc, 0x1000, v2
	s_mov_b64 s[0:1], 0x1800
	s_nop 0
	v_addc_co_u32_e32 v37, vcc, 0, v3, vcc
	v_lshl_add_u64 v[42:43], v[2:3], 0, s[0:1]
	global_load_dwordx4 v[2:5], v34, s[60:61] offset:16
	global_load_dwordx4 v[6:9], v34, s[60:61]
	global_load_dwordx4 v[10:13], v34, s[60:61] offset:2064
	global_load_dwordx4 v[14:17], v34, s[60:61] offset:2048
	global_load_dwordx4 v[18:21], v[38:39], off offset:16
	global_load_dwordx4 v[22:25], v[36:37], off
	global_load_dwordx4 v[26:29], v[36:37], off offset:2048
	global_load_dwordx4 v[30:33], v[42:43], off offset:16
	v_readlane_b32 s42, v255, 3
	v_readlane_b32 s43, v255, 4
	s_add_u32 s22, s42, 0x100000
	s_addc_u32 s23, s43, 0
	s_add_i32 s2, 0, 0x10000
	v_lshlrev_b32_e32 v40, 4, v1
	v_add_u32_e32 v77, s2, v40
	s_add_i32 s2, 0, 0x10400
	v_add_u32_e32 v78, s2, v40
	s_add_i32 s2, 0, 0x12000
	v_add_u32_e32 v79, s2, v40
	s_add_i32 s2, 0, 0x12400
	v_add_u32_e32 v80, s2, v40
	s_add_i32 s2, 0, 0x14000
	v_add_u32_e32 v81, s2, v40
	s_add_i32 s2, 0, 0x14400
	v_add_u32_e32 v82, s2, v40
	s_add_i32 s2, 0, 0x16000
	v_add_u32_e32 v83, s2, v40
	s_add_i32 s2, 0, 0x16400
	v_add_u32_e32 v84, s2, v40
	s_add_i32 s2, 0, 0x18000
	v_add_u32_e32 v85, s2, v40
	s_add_i32 s2, 0, 0x18400
	v_add_u32_e32 v86, s2, v40
	s_add_i32 s2, 0, 0x1a000
	v_add_u32_e32 v87, s2, v40
	s_add_i32 s2, 0, 0x1a400
	v_add_u32_e32 v88, s2, v40
	s_add_i32 s2, 0, 0x1c000
	v_add_u32_e32 v89, s2, v40
	s_add_i32 s2, 0, 0x1c400
	v_add_u32_e32 v90, s2, v40
	s_add_i32 s2, 0, 0x1e000
	v_add_u32_e32 v91, s2, v40
	s_add_i32 s2, 0, 0x1e400
	v_add_u32_e32 v92, s2, v40
	s_add_i32 s2, 0, 0x10800
	v_add_u32_e32 v93, s2, v40
	s_add_i32 s2, 0, 0x10c00
	v_add_u32_e32 v94, s2, v40
	s_add_i32 s2, 0, 0x12800
	v_add_u32_e32 v95, s2, v40
	s_add_i32 s2, 0, 0x12c00
	v_add_u32_e32 v96, s2, v40
	s_add_i32 s2, 0, 0x14800
	v_add_u32_e32 v97, s2, v40
	s_add_i32 s2, 0, 0x14c00
	v_add_u32_e32 v98, s2, v40
	s_add_i32 s2, 0, 0x16800
	v_add_u32_e32 v99, s2, v40
	s_add_i32 s2, 0, 0x16c00
	v_add_u32_e32 v100, s2, v40
	s_add_i32 s2, 0, 0x18800
	v_add_u32_e32 v101, s2, v40
	s_add_i32 s2, 0, 0x18c00
	v_add_u32_e32 v102, s2, v40
	s_add_i32 s2, 0, 0x1a800
	v_add_u32_e32 v103, s2, v40
	s_add_i32 s2, 0, 0x1ac00
	v_add_u32_e32 v104, s2, v40
	s_add_i32 s2, 0, 0x1c800
	v_add_u32_e32 v105, s2, v40
	s_add_i32 s2, 0, 0x1cc00
	v_add_u32_e32 v106, s2, v40
	s_add_i32 s2, 0, 0x1e800
	v_add_u32_e32 v107, s2, v40
	s_add_i32 s2, 0, 0x1ec00
	v_add_u32_e32 v108, s2, v40
	s_add_i32 s2, 0, 0x11000
	v_add_u32_e32 v109, s2, v40
	s_add_i32 s2, 0, 0x11400
	v_add_u32_e32 v110, s2, v40
	s_add_i32 s2, 0, 0x13000
	v_add_u32_e32 v111, s2, v40
	s_add_i32 s2, 0, 0x13400
	v_add_u32_e32 v112, s2, v40
	s_add_i32 s2, 0, 0x15000
	v_add_u32_e32 v113, s2, v40
	s_add_i32 s2, 0, 0x15400
	v_add_u32_e32 v114, s2, v40
	s_add_i32 s2, 0, 0x17000
	v_add_u32_e32 v115, s2, v40
	s_add_i32 s2, 0, 0x17400
	v_add_u32_e32 v116, s2, v40
	s_add_i32 s2, 0, 0x19000
	v_add_u32_e32 v117, s2, v40
	s_add_i32 s2, 0, 0x19400
	v_add_u32_e32 v118, s2, v40
	s_add_i32 s2, 0, 0x1b000
	v_add_u32_e32 v119, s2, v40
	s_add_i32 s2, 0, 0x1b400
	v_add_u32_e32 v120, s2, v40
	s_add_i32 s2, 0, 0x1d000
	v_readlane_b32 s41, v255, 2
	v_add_u32_e32 v121, s2, v40
	s_add_i32 s2, 0, 0x1d400
	s_ashr_i32 s19, s18, 31
	v_add_u32_e32 v122, s2, v40
	s_add_i32 s2, 0, 0x1f000
	s_add_i32 s20, 0, 0x1f400
	s_add_i32 s24, 0, 0x11800
	s_add_i32 s25, 0, 0x11c00
	s_add_i32 s26, 0, 0x13800
	s_add_i32 s27, 0, 0x13c00
	s_add_i32 s28, 0, 0x15800
	s_add_i32 s29, 0, 0x15c00
	s_add_i32 s31, 0, 0x17800
	s_add_i32 s33, 0, 0x17c00
	s_add_i32 s34, 0, 0x19800
	s_add_i32 s35, 0, 0x19c00
	s_add_i32 s36, 0, 0x1b800
	s_add_i32 s37, 0, 0x1bc00
	s_add_i32 s38, 0, 0x1d800
	s_add_i32 s39, 0, 0x1dc00
	s_add_i32 s40, 0, 0x1f800
	s_add_i32 s41, 0, 0x1fc00
	s_lshl_b64 s[16:17], s[18:19], 12
	s_add_u32 s16, s42, s16
	v_mov_b32_e32 v41, v35
	s_addc_u32 s17, s43, s17
	v_lshl_add_u64 v[36:37], s[16:17], 0, v[40:41]
	s_mov_b64 s[16:17], 0x7b00c00
	v_lshl_add_u64 v[68:69], v[36:37], 0, s[16:17]
	s_lshl_b64 s[16:17], s[18:19], 13
	v_readlane_b32 s49, v255, 22
	s_add_u32 s16, s48, s16
	s_addc_u32 s17, s49, s17
	v_mov_b32_e32 v67, v35
	v_add_u32_e32 v125, s24, v40
	v_add_u32_e32 v126, s25, v40
	s_mov_b64 s[24:25], 0x1810
	v_lshl_add_u64 v[34:35], s[16:17], 0, v[34:35]
	v_lshl_add_u64 v[70:71], v[34:35], 0, s[24:25]
	v_readlane_b32 s52, v255, 25
	v_readlane_b32 s53, v255, 26
	s_movk_i32 s24, 0xe7f0
	v_mbcnt_lo_u32_b32 v34, -1, 0
	s_mov_b32 s21, 0
	v_cmp_gt_u32_e64 s[0:1], 8, v1
	v_add_u32_e32 v123, s2, v40
	v_cmp_eq_u32_e64 s[2:3], 1, v1
	v_cmp_eq_u32_e64 s[4:5], 2, v1
	v_cmp_eq_u32_e64 s[6:7], 3, v1
	v_cmp_eq_u32_e64 s[8:9], 4, v1
	v_cmp_eq_u32_e64 s[10:11], 5, v1
	v_cmp_eq_u32_e64 s[12:13], 6, v1
	v_cmp_eq_u32_e64 s[14:15], 7, v1
	v_add_u32_e32 v124, s20, v40
	v_add_u32_e32 v127, s26, v40
	v_add_u32_e32 v128, s27, v40
	v_add_u32_e32 v129, s28, v40
	v_add_u32_e32 v130, s29, v40
	v_add_u32_e32 v131, s31, v40
	v_add_u32_e32 v132, s33, v40
	v_add_u32_e32 v133, s34, v40
	v_add_u32_e32 v134, s35, v40
	v_add_u32_e32 v135, s36, v40
	v_add_u32_e32 v136, s37, v40
	v_add_u32_e32 v137, s38, v40
	v_add_u32_e32 v138, s39, v40
	v_add_u32_e32 v139, s40, v40
	v_add_u32_e32 v140, s41, v40
	s_mov_b32 s25, -1
	s_mov_b32 s19, 0xf800000
	s_mov_b32 s31, 0xbfb8aa3b
	s_mov_b32 s33, 0xb2a5705f
	s_mov_b32 s34, 0x42ce8ed0
	s_mov_b32 s35, 0xc2b17218
	s_mov_b32 s36, 0x7f800000
	s_mov_b32 s37, 0x3f2aaaab
	s_mov_b32 s38, 0x3f317218
	s_mov_b32 s39, 0x33800000
	s_mov_b64 s[26:27], 0x800000
	s_mov_b64 s[28:29], 0x1000000
	v_mbcnt_hi_u32_b32 v141, -1, v34
	s_mov_b32 s40, s18
	v_mov_b32_e32 v142, 0x358637bd
	v_mov_b32_e32 v143, 0x260
	v_mov_b32_e32 v144, 0x3ecc95a3
	v_mov_b32_e32 v145, 0x7f800000
	v_lshl_add_u64 v[72:73], s[52:53], 0, v[66:67]
	v_mov_b32_e32 v74, 0x3f317218
	v_readlane_b32 s50, v255, 23
	v_readlane_b32 s51, v255, 24
	v_readlane_b32 s54, v255, 27
	v_readlane_b32 s55, v255, 28
	v_readlane_b32 s56, v255, 29
	v_readlane_b32 s57, v255, 30
	v_readlane_b32 s58, v255, 31
	v_readlane_b32 s59, v255, 32
	v_readlane_b32 s62, v255, 35
	v_readlane_b32 s63, v255, 36
	v_readlane_b32 s44, v255, 5
	v_readlane_b32 s45, v255, 6
	v_readlane_b32 s46, v255, 7
	v_readlane_b32 s47, v255, 8
	s_mov_b64 vcc, exec
	s_mov_b64 exec, s[0:1]
	global_load_dword v178, v[72:73], off
	s_mov_b64 exec, vcc
	v_add_co_u32_e32 v214, vcc, 0xfffff000, v70
	v_addc_co_u32_e32 v215, vcc, -1, v71, vcc
	global_load_dwordx4 v[180:183], v[214:215], off offset:-2048 nt
	global_load_dwordx4 v[184:187], v[70:71], off offset:-2064 nt
	global_load_dwordx4 v[188:191], v[70:71], off offset:-4096 nt
	global_load_dwordx4 v[192:195], v[70:71], off offset:-2048 nt
	global_load_dwordx4 v[196:199], v[70:71], off nt
	global_load_dwordx4 v[200:203], v[70:71], off offset:-16 nt
	global_load_dwordx4 v[204:207], v[214:215], off offset:-16 nt
	global_load_dwordx4 v[208:211], v[214:215], off offset:-2064 nt
	s_branch .LBB0_25

.LBB0_25:
	s_waitcnt vmcnt(0) lgkmcnt(0)
	v_mov_b32_e32 v58, v180
	v_mov_b32_e32 v59, v181
	v_mov_b32_e32 v60, v182
	v_mov_b32_e32 v61, v183
	v_mov_b32_e32 v46, v184
	v_mov_b32_e32 v47, v185
	v_mov_b32_e32 v48, v186
	v_mov_b32_e32 v49, v187
	v_mov_b32_e32 v50, v188
	v_mov_b32_e32 v51, v189
	v_mov_b32_e32 v52, v190
	v_mov_b32_e32 v53, v191
	v_mov_b32_e32 v42, v192
	v_mov_b32_e32 v43, v193
	v_mov_b32_e32 v44, v194
	v_mov_b32_e32 v45, v195
	v_mov_b32_e32 v34, v196
	v_mov_b32_e32 v35, v197
	v_mov_b32_e32 v36, v198
	v_mov_b32_e32 v37, v199
	v_mov_b32_e32 v38, v200
	v_mov_b32_e32 v39, v201
	v_mov_b32_e32 v40, v202
	v_mov_b32_e32 v41, v203
	v_mov_b32_e32 v54, v204
	v_mov_b32_e32 v55, v205
	v_mov_b32_e32 v56, v206
	v_mov_b32_e32 v57, v207
	v_mov_b32_e32 v62, v208
	v_mov_b32_e32 v63, v209
	v_mov_b32_e32 v64, v210
	v_mov_b32_e32 v65, v211
	s_cmpk_gt_i32 s40, 0x17ff
	s_cbranch_scc1 .Lp0_nopf
	v_lshl_add_u64 v[212:213], v[70:71], 0, s[28:29]
	v_add_co_u32_e32 v214, vcc, 0xfffff000, v212
	v_addc_co_u32_e32 v215, vcc, -1, v213, vcc
	global_load_dwordx4 v[180:183], v[214:215], off offset:-2048 nt
	global_load_dwordx4 v[184:187], v[212:213], off offset:-2064 nt
	global_load_dwordx4 v[188:191], v[212:213], off offset:-4096 nt
	global_load_dwordx4 v[192:195], v[212:213], off offset:-2048 nt
	global_load_dwordx4 v[196:199], v[212:213], off nt
	global_load_dwordx4 v[200:203], v[212:213], off offset:-16 nt
	global_load_dwordx4 v[204:207], v[214:215], off offset:-16 nt
	global_load_dwordx4 v[208:211], v[214:215], off offset:-2064 nt
.Lp0_nopf:
	s_cmp_eq_u32 s40, s18
	s_cbranch_scc1 .Lp0_nost
	s_and_saveexec_b64 s[16:17], s[0:1]
	global_store_dword v[216:217], v218, off
	s_or_b64 exec, exec, s[16:17]
.Lp0_nost:
	v_and_b32_e32 v67, 64, v141
	v_xor_b32_e32 v75, 1, v141
	v_add_u32_e32 v170, 64, v67
	v_cmp_lt_i32_e32 vcc, v75, v170
	v_mov_b32_e32 v149, v59
	v_mov_b32_e32 v147, v58
	v_mul_f32_e32 v146, v53, v53
	v_pk_mul_f32 v[150:151], v[44:45], v[44:45]
	v_pk_mul_f32 v[152:153], v[42:43], v[42:43]
	v_mul_f32_e32 v148, v39, v39
	v_mul_f32_e32 v154, v41, v41
	v_mov_b32_e32 v155, v60
	v_mov_b32_e32 v157, v61
	v_pk_mov_b32 v[158:159], v[152:153], v[150:151] op_sel:[1,0]
	v_mov_b32_e32 v153, v151
	v_pk_fma_f32 v[162:163], v[38:39], v[38:39], v[148:149] op_sel_hi:[1,1,0]
	v_mov_b32_e32 v148, v63
	v_mov_b32_e32 v156, v65
	v_pk_fma_f32 v[160:161], v[52:53], v[52:53], v[146:147] op_sel_hi:[1,1,0]
	v_pk_fma_f32 v[164:165], v[40:41], v[40:41], v[154:155] op_sel_hi:[1,1,0]
	v_pk_mul_f32 v[166:167], v[56:57], v[56:57]
	v_pk_mul_f32 v[168:169], v[54:55], v[54:55]
	v_mov_b32_e32 v146, v62
	v_mov_b32_e32 v154, v64
	v_pk_add_f32 v[152:153], v[158:159], v[152:153]
	v_pk_mul_f32 v[148:149], v[148:149], v[148:149]
	v_pk_mul_f32 v[156:157], v[156:157], v[156:157]
	v_pk_mov_b32 v[158:159], v[168:169], v[166:167] op_sel:[1,0]
	v_mov_b32_e32 v169, v167
	v_pk_fma_f32 v[146:147], v[146:147], v[146:147], v[148:149]
	v_pk_add_f32 v[148:149], v[152:153], v[152:153] op_sel:[0,1] op_sel_hi:[1,0]
	v_pk_fma_f32 v[152:153], v[154:155], v[154:155], v[156:157]
	v_mul_f32_e32 v76, v51, v51
	v_pk_add_f32 v[154:155], v[158:159], v[168:169]
	v_pk_add_f32 v[146:147], v[146:147], v[152:153]
	v_cndmask_b32_e32 v67, v141, v75, vcc
	v_mul_f32_e32 v75, v48, v48
	v_mul_f32_e32 v171, v49, v49
	v_mul_f32_e32 v174, v46, v46
	v_mul_f32_e32 v175, v47, v47
	v_pk_fma_f32 v[150:151], v[50:51], v[50:51], v[76:77] op_sel_hi:[1,1,0]
	v_pk_add_f32 v[152:153], v[154:155], v[154:155] op_sel:[0,1] op_sel_hi:[1,0]
	v_pk_add_f32 v[146:147], v[146:147], v[146:147] op_sel:[0,1] op_sel_hi:[1,0]
	v_mov_b32_e32 v151, v75
	v_mov_b32_e32 v161, v171
	v_mov_b32_e32 v153, v175
	v_mov_b32_e32 v147, v174
	v_pk_add_f32 v[150:151], v[150:151], v[160:161]
	v_pk_add_f32 v[146:147], v[146:147], v[152:153]
	v_mul_f32_e32 v172, v36, v36
	v_pk_add_f32 v[146:147], v[146:147], v[150:151]
	v_mul_f32_e32 v173, v37, v37
	v_mul_f32_e32 v176, v34, v34
	v_mul_f32_e32 v177, v35, v35
	v_pk_add_f32 v[146:147], v[146:147], v[146:147] op_sel:[0,1] op_sel_hi:[1,0]
	v_mov_b32_e32 v163, v172
	v_mov_b32_e32 v165, v173
	v_mov_b32_e32 v149, v177
	v_mov_b32_e32 v147, v176
	v_pk_add_f32 v[160:161], v[162:163], v[164:165]
	v_pk_add_f32 v[146:147], v[146:147], v[148:149]
	v_lshlrev_b32_e32 v67, 2, v67
	v_pk_add_f32 v[146:147], v[146:147], v[160:161]
	s_nop 0
	v_add_f32_e32 v75, v146, v147
	ds_bpermute_b32 v76, v67, v75
	v_xor_b32_e32 v146, 2, v141
	v_cmp_lt_i32_e32 vcc, v146, v170
	s_waitcnt lgkmcnt(0)
	v_add_f32_e32 v75, v75, v76
	v_cndmask_b32_e32 v146, v141, v146, vcc
	v_lshlrev_b32_e32 v149, 2, v146
	ds_bpermute_b32 v76, v149, v75
	v_xor_b32_e32 v146, 4, v141
	v_cmp_lt_i32_e32 vcc, v146, v170
	s_waitcnt lgkmcnt(0)
	v_add_f32_e32 v75, v75, v76
	v_cndmask_b32_e32 v146, v141, v146, vcc
	v_lshlrev_b32_e32 v148, 2, v146
	ds_bpermute_b32 v76, v148, v75
	v_xor_b32_e32 v146, 8, v141
	v_cmp_lt_i32_e32 vcc, v146, v170
	s_waitcnt lgkmcnt(0)
	v_add_f32_e32 v75, v75, v76
	v_cndmask_b32_e32 v146, v141, v146, vcc
	v_lshlrev_b32_e32 v147, 2, v146
	ds_bpermute_b32 v76, v147, v75
	v_xor_b32_e32 v146, 16, v141
	v_cmp_lt_i32_e32 vcc, v146, v170
	s_waitcnt lgkmcnt(0)
	v_add_f32_e32 v76, v75, v76
	v_cndmask_b32_e32 v146, v141, v146, vcc
	v_lshlrev_b32_e32 v146, 2, v146
	ds_bpermute_b32 v150, v146, v76
	v_xor_b32_e32 v75, 32, v141
	v_cmp_lt_i32_e32 vcc, v75, v170
	s_waitcnt lgkmcnt(0)
	v_add_f32_e32 v76, v76, v150
	v_cndmask_b32_e32 v75, v141, v75, vcc
	v_lshlrev_b32_e32 v75, 2, v75
	ds_bpermute_b32 v150, v75, v76
	s_waitcnt lgkmcnt(0)
	v_add_f32_e32 v76, v76, v150
	v_fmamk_f32 v76, v76, 0x3a000000, v142
	v_mul_f32_e32 v150, 0x4f800000, v76
	v_cmp_gt_f32_e32 vcc, s19, v76
	s_nop 1
	v_cndmask_b32_e32 v76, v76, v150, vcc
	v_sqrt_f32_e32 v158, v76
	ds_read_b128 v[150:153], v77
	ds_read_b128 v[154:157], v78
	v_add_u32_e32 v159, -1, v158
	v_add_u32_e32 v160, 1, v158
	v_fma_f32 v161, -v159, v158, v76
	v_fma_f32 v162, -v160, v158, v76
	v_cmp_ge_f32_e64 s[16:17], 0, v161
	s_nop 1
	v_cndmask_b32_e64 v158, v158, v159, s[16:17]
	v_cmp_lt_f32_e64 s[16:17], 0, v162
	s_nop 1
	v_cndmask_b32_e64 v158, v158, v160, s[16:17]
	v_mul_f32_e32 v159, 0x37800000, v158
	v_cndmask_b32_e32 v158, v158, v159, vcc
	v_cmp_class_f32_e32 vcc, v76, v143
	s_nop 1
	v_cndmask_b32_e32 v76, v158, v76, vcc
	v_div_scale_f32 v162, s[16:17], v76, v76, 1.0
	v_rcp_f32_e32 v163, v162
	v_div_scale_f32 v164, vcc, 1.0, v76, 1.0
	ds_read_b128 v[158:161], v79
	v_fma_f32 v165, -v162, v163, 1.0
	v_fmac_f32_e32 v163, v165, v163
	v_mul_f32_e32 v165, v164, v163
	v_fma_f32 v166, -v162, v165, v164
	v_fmac_f32_e32 v165, v166, v163
	v_fma_f32 v162, -v162, v165, v164
	v_div_fmas_f32 v162, v162, v163, v165
	v_div_fixup_f32 v76, v162, v76, 1.0
	v_pk_mul_f32 v[62:63], v[76:77], v[62:63] op_sel_hi:[0,1]
	v_pk_mul_f32 v[64:65], v[76:77], v[64:65] op_sel_hi:[0,1]
	v_pk_mul_f32 v[58:59], v[76:77], v[58:59] op_sel_hi:[0,1]
	v_pk_mul_f32 v[60:61], v[76:77], v[60:61] op_sel_hi:[0,1]
	v_pk_mul_f32 v[162:163], v[64:65], v[8:9]
	v_pk_mul_f32 v[164:165], v[62:63], v[6:7]
	v_pk_mul_f32 v[166:167], v[60:61], v[4:5]
	v_pk_mul_f32 v[168:169], v[58:59], v[2:3]
	v_cvt_pk_bf16_f32 v58, v164, v165
	v_cvt_pk_bf16_f32 v59, v162, v163
	v_cvt_pk_bf16_f32 v60, v168, v169
	v_cvt_pk_bf16_f32 v61, v166, v167
	global_store_dwordx4 v[68:69], v[58:61], off offset:-3072
	ds_read_b128 v[58:61], v80
	s_waitcnt lgkmcnt(3)
	v_mul_f32_e32 v153, v163, v153
	v_fmac_f32_e32 v153, v162, v152
	s_waitcnt lgkmcnt(2)
	v_mul_f32_e32 v152, v167, v157
	ds_read_b128 v[62:65], v81
	v_fmac_f32_e32 v152, v166, v156
	s_waitcnt lgkmcnt(1)
	v_mul_f32_e32 v156, v169, v59
	v_mul_f32_e32 v157, v167, v61
	v_mul_f32_e32 v151, v165, v151
	v_fmac_f32_e32 v156, v168, v58
	v_fmac_f32_e32 v157, v166, v60
	ds_read_b128 v[58:61], v82
	v_fmac_f32_e32 v151, v164, v150
	v_mul_f32_e32 v150, v169, v155
	v_fmac_f32_e32 v150, v168, v154
	v_mul_f32_e32 v154, v165, v159
	v_fmac_f32_e32 v154, v164, v158
	s_waitcnt lgkmcnt(1)
	v_mul_f32_e32 v158, v165, v63
	v_mul_f32_e32 v159, v163, v65
	v_fmac_f32_e32 v158, v164, v62
	v_fmac_f32_e32 v159, v162, v64
	ds_read_b128 v[62:65], v83
	v_add_f32_e32 v151, v151, v153
	v_add_f32_e32 v150, v150, v152
	s_waitcnt lgkmcnt(1)
	v_mul_f32_e32 v152, v169, v59
	v_mul_f32_e32 v153, v167, v61
	v_fmac_f32_e32 v152, v168, v58
	v_fmac_f32_e32 v153, v166, v60
	ds_read_b128 v[58:61], v84
	v_mul_f32_e32 v155, v163, v161
	v_fmac_f32_e32 v155, v162, v160
	v_add_f32_e32 v150, v151, v150
	v_add_f32_e32 v151, v154, v155
	s_waitcnt lgkmcnt(1)
	v_mul_f32_e32 v154, v165, v63
	v_fmac_f32_e32 v154, v164, v62
	v_mul_f32_e32 v155, v163, v65
	v_add_f32_e32 v62, v156, v157
	v_fmac_f32_e32 v155, v162, v64
	v_add_f32_e32 v151, v151, v62
	s_waitcnt lgkmcnt(0)
	v_mul_f32_e32 v156, v169, v59
	v_mul_f32_e32 v157, v167, v61
	ds_read_b128 v[62:65], v85
	v_fmac_f32_e32 v156, v168, v58
	v_fmac_f32_e32 v157, v166, v60
	ds_read_b128 v[58:61], v86
	v_add_f32_e32 v158, v158, v159
	v_add_f32_e32 v152, v152, v153
	s_waitcnt lgkmcnt(1)
	v_mul_f32_e32 v153, v165, v63
	v_mul_f32_e32 v159, v163, v65
	v_fmac_f32_e32 v153, v164, v62
	v_fmac_f32_e32 v159, v162, v64
	v_add_f32_e32 v154, v154, v155
	s_waitcnt lgkmcnt(0)
	v_mul_f32_e32 v155, v169, v59
	ds_read_b128 v[62:65], v87
	v_add_f32_e32 v152, v158, v152
	v_fmac_f32_e32 v155, v168, v58
	v_mul_f32_e32 v158, v167, v61
	v_add_f32_e32 v58, v156, v157
	v_fmac_f32_e32 v158, v166, v60
	v_add_f32_e32 v154, v154, v58
	ds_read_b128 v[58:61], v88
	s_waitcnt lgkmcnt(1)
	v_mul_f32_e32 v63, v165, v63
	v_fmac_f32_e32 v63, v164, v62
	v_mul_f32_e32 v62, v163, v65
	v_fmac_f32_e32 v62, v162, v64
	v_add_f32_e32 v64, v153, v159
	v_add_f32_e32 v65, v155, v158
	s_waitcnt lgkmcnt(0)
	v_mul_f32_e32 v153, v169, v59
	v_mul_f32_e32 v155, v167, v61
	v_fmac_f32_e32 v153, v168, v58
	v_fmac_f32_e32 v155, v166, v60
	ds_read_b128 v[58:61], v89
	v_add_f32_e32 v156, v64, v65
	v_add_f32_e32 v157, v63, v62
	ds_read_b128 v[62:65], v90
	v_pk_mul_f32 v[54:55], v[76:77], v[54:55] op_sel_hi:[0,1]
	s_waitcnt lgkmcnt(1)
	v_mul_f32_e32 v158, v165, v59
	v_fmac_f32_e32 v158, v164, v58
	v_mul_f32_e32 v159, v163, v61
	v_add_f32_e32 v58, v153, v155
	v_fmac_f32_e32 v159, v162, v60
	v_add_f32_e32 v153, v157, v58
	ds_read_b128 v[58:61], v91
	s_waitcnt lgkmcnt(1)
	v_mul_f32_e32 v155, v169, v63
	v_mul_f32_e32 v157, v167, v65
	v_fmac_f32_e32 v155, v168, v62
	v_fmac_f32_e32 v157, v166, v64
	ds_read_b128 v[62:65], v92
	s_waitcnt lgkmcnt(1)
	v_mul_f32_e32 v59, v165, v59
	v_fmac_f32_e32 v59, v164, v58
	v_mul_f32_e32 v58, v163, v61
	v_add_f32_e32 v158, v158, v159
	v_fmac_f32_e32 v58, v162, v60
	v_add_f32_e32 v60, v155, v157
	v_add_f32_e32 v60, v158, v60
	v_add_f32_e32 v155, 0, v60
	v_add_f32_e32 v58, v59, v58
	s_waitcnt lgkmcnt(0)
	v_mul_f32_e32 v59, v169, v63
	v_mul_f32_e32 v60, v167, v65
	v_fmac_f32_e32 v59, v168, v62
	v_fmac_f32_e32 v60, v166, v64
	v_add_f32_e32 v59, v59, v60
	v_add_f32_e32 v58, v58, v59
	v_pk_mul_f32 v[56:57], v[76:77], v[56:57] op_sel_hi:[0,1]
	v_add_f32_e32 v157, 0, v58
	v_pk_mul_f32 v[58:59], v[56:57], v[16:17]
	v_pk_mul_f32 v[60:61], v[54:55], v[14:15]
	v_pk_mul_f32 v[50:51], v[76:77], v[50:51] op_sel_hi:[0,1]
	v_pk_mul_f32 v[52:53], v[76:77], v[52:53] op_sel_hi:[0,1]
	ds_read_b128 v[54:57], v93
	v_pk_mul_f32 v[62:63], v[52:53], v[12:13]
	v_pk_mul_f32 v[64:65], v[50:51], v[10:11]
	v_cvt_pk_bf16_f32 v50, v60, v61
	v_cvt_pk_bf16_f32 v51, v58, v59
	v_cvt_pk_bf16_f32 v52, v64, v65
	v_cvt_pk_bf16_f32 v53, v62, v63
	global_store_dwordx4 v[68:69], v[50:53], off offset:-2048
	ds_read_b128 v[50:53], v94
	s_waitcnt lgkmcnt(1)
	v_mul_f32_e32 v55, v61, v55
	v_fmac_f32_e32 v55, v60, v54
	v_mul_f32_e32 v54, v59, v57
	v_fmac_f32_e32 v54, v58, v56
	v_add_f32_e32 v54, v55, v54
	s_waitcnt lgkmcnt(0)
	v_mul_f32_e32 v55, v65, v51
	v_mul_f32_e32 v56, v63, v53
	v_fmac_f32_e32 v55, v64, v50
	v_fmac_f32_e32 v56, v62, v52
	v_add_f32_e32 v55, v55, v56
	v_add_f32_e32 v150, 0, v150
	v_add_f32_e32 v54, v54, v55
	ds_read_b128 v[50:53], v95
	v_add_f32_e32 v150, v150, v54
	ds_read_b128 v[54:57], v96
	v_add_f32_e32 v151, 0, v151
	v_add_f32_e32 v152, 0, v152
	s_waitcnt lgkmcnt(1)
	v_mul_f32_e32 v51, v61, v51
	v_fmac_f32_e32 v51, v60, v50
	s_waitcnt lgkmcnt(0)
	v_mul_f32_e32 v55, v65, v55
	v_mul_f32_e32 v50, v59, v53
	v_fmac_f32_e32 v55, v64, v54
	v_mul_f32_e32 v54, v63, v57
	v_fmac_f32_e32 v50, v58, v52
	v_fmac_f32_e32 v54, v62, v56
	v_add_f32_e32 v158, v51, v50
	v_add_f32_e32 v54, v55, v54
	v_add_f32_e32 v54, v158, v54
	ds_read_b128 v[50:53], v97
	v_add_f32_e32 v151, v151, v54
	ds_read_b128 v[54:57], v98
	v_add_f32_e32 v154, 0, v154
	v_add_f32_e32 v156, 0, v156
	s_waitcnt lgkmcnt(1)
	v_mul_f32_e32 v51, v61, v51
	v_fmac_f32_e32 v51, v60, v50
	s_waitcnt lgkmcnt(0)
	v_mul_f32_e32 v55, v65, v55
	v_mul_f32_e32 v50, v59, v53
	v_fmac_f32_e32 v55, v64, v54
	v_mul_f32_e32 v54, v63, v57
	v_fmac_f32_e32 v50, v58, v52
	v_fmac_f32_e32 v54, v62, v56
	v_add_f32_e32 v158, v51, v50
	v_add_f32_e32 v54, v55, v54
	v_add_f32_e32 v54, v158, v54
	ds_read_b128 v[50:53], v99
	v_add_f32_e32 v152, v152, v54
	ds_read_b128 v[54:57], v100
	v_add_f32_e32 v153, 0, v153
	v_pk_mul_f32 v[46:47], v[76:77], v[46:47] op_sel_hi:[0,1]
	s_waitcnt lgkmcnt(1)
	v_mul_f32_e32 v51, v61, v51
	v_fmac_f32_e32 v51, v60, v50
	s_waitcnt lgkmcnt(0)
	v_mul_f32_e32 v55, v65, v55
	v_mul_f32_e32 v50, v59, v53
	v_fmac_f32_e32 v55, v64, v54
	v_mul_f32_e32 v54, v63, v57
	v_fmac_f32_e32 v50, v58, v52
	v_fmac_f32_e32 v54, v62, v56
	v_add_f32_e32 v158, v51, v50
	v_add_f32_e32 v54, v55, v54
	v_add_f32_e32 v54, v158, v54
	ds_read_b128 v[50:53], v101
	v_add_f32_e32 v154, v154, v54
	ds_read_b128 v[54:57], v102
	v_pk_mul_f32 v[48:49], v[76:77], v[48:49] op_sel_hi:[0,1]
	v_pk_mul_f32 v[42:43], v[76:77], v[42:43] op_sel_hi:[0,1]
	s_waitcnt lgkmcnt(1)
	v_mul_f32_e32 v51, v61, v51
	v_fmac_f32_e32 v51, v60, v50
	s_waitcnt lgkmcnt(0)
	v_mul_f32_e32 v55, v65, v55
	v_mul_f32_e32 v50, v59, v53
	v_fmac_f32_e32 v55, v64, v54
	v_mul_f32_e32 v54, v63, v57
	v_fmac_f32_e32 v50, v58, v52
	v_fmac_f32_e32 v54, v62, v56
	v_add_f32_e32 v158, v51, v50
	v_add_f32_e32 v54, v55, v54
	v_add_f32_e32 v54, v158, v54
	ds_read_b128 v[50:53], v103
	v_add_f32_e32 v156, v156, v54
	ds_read_b128 v[54:57], v104
	v_pk_mul_f32 v[44:45], v[76:77], v[44:45] op_sel_hi:[0,1]
	v_pk_mul_f32 v[34:35], v[76:77], v[34:35] op_sel_hi:[0,1]
	s_waitcnt lgkmcnt(1)
	v_mul_f32_e32 v51, v61, v51
	v_fmac_f32_e32 v51, v60, v50
	s_waitcnt lgkmcnt(0)
	v_mul_f32_e32 v55, v65, v55
	v_mul_f32_e32 v50, v59, v53
	v_fmac_f32_e32 v55, v64, v54
	v_mul_f32_e32 v54, v63, v57
	v_fmac_f32_e32 v50, v58, v52
	v_fmac_f32_e32 v54, v62, v56
	v_add_f32_e32 v158, v51, v50
	v_add_f32_e32 v54, v55, v54
	ds_read_b128 v[50:53], v105
	v_add_f32_e32 v54, v158, v54
	v_add_f32_e32 v153, v153, v54
	ds_read_b128 v[54:57], v106
	v_pk_mul_f32 v[36:37], v[76:77], v[36:37] op_sel_hi:[0,1]
	s_waitcnt lgkmcnt(1)
	v_mul_f32_e32 v51, v61, v51
	v_fmac_f32_e32 v51, v60, v50
	v_mul_f32_e32 v50, v59, v53
	s_waitcnt lgkmcnt(0)
	v_mul_f32_e32 v55, v65, v55
	v_fmac_f32_e32 v50, v58, v52
	v_fmac_f32_e32 v55, v64, v54
	v_mul_f32_e32 v54, v63, v57
	v_add_f32_e32 v158, v51, v50
	v_fmac_f32_e32 v54, v62, v56
	ds_read_b128 v[50:53], v107
	v_add_f32_e32 v54, v55, v54
	v_add_f32_e32 v54, v158, v54
	v_add_f32_e32 v155, v155, v54
	ds_read_b128 v[54:57], v108
	s_waitcnt lgkmcnt(1)
	v_mul_f32_e32 v51, v61, v51
	v_fmac_f32_e32 v51, v60, v50
	v_mul_f32_e32 v50, v59, v53
	v_fmac_f32_e32 v50, v58, v52
	v_add_f32_e32 v50, v51, v50
	s_waitcnt lgkmcnt(0)
	v_mul_f32_e32 v51, v65, v55
	v_mul_f32_e32 v52, v63, v57
	v_fmac_f32_e32 v51, v64, v54
	v_fmac_f32_e32 v52, v62, v56
	v_add_f32_e32 v51, v51, v52
	v_add_f32_e32 v50, v50, v51
	v_add_f32_e32 v58, v157, v50
	v_pk_mul_f32 v[50:51], v[48:49], v[24:25]
	v_pk_mul_f32 v[52:53], v[46:47], v[22:23]
	ds_read_b128 v[46:49], v109
	v_pk_mul_f32 v[54:55], v[44:45], v[20:21]
	v_pk_mul_f32 v[56:57], v[42:43], v[18:19]
	v_cvt_pk_bf16_f32 v42, v52, v53
	v_cvt_pk_bf16_f32 v43, v50, v51
	v_cvt_pk_bf16_f32 v44, v56, v57
	v_cvt_pk_bf16_f32 v45, v54, v55
	global_store_dwordx4 v[68:69], v[42:45], off offset:-1024
	ds_read_b128 v[42:45], v110
	s_waitcnt lgkmcnt(1)
	v_mul_f32_e32 v47, v53, v47
	v_fmac_f32_e32 v47, v52, v46
	v_mul_f32_e32 v46, v51, v49
	v_fmac_f32_e32 v46, v50, v48
	v_add_f32_e32 v46, v47, v46
	s_waitcnt lgkmcnt(0)
	v_mul_f32_e32 v47, v57, v43
	v_mul_f32_e32 v48, v55, v45
	v_fmac_f32_e32 v47, v56, v42
	v_fmac_f32_e32 v48, v54, v44
	v_add_f32_e32 v47, v47, v48
	v_add_f32_e32 v46, v46, v47
	ds_read_b128 v[42:45], v111
	v_add_f32_e32 v59, v150, v46
	ds_read_b128 v[46:49], v112
	s_waitcnt lgkmcnt(1)
	v_mul_f32_e32 v43, v53, v43
	v_fmac_f32_e32 v43, v52, v42
	s_waitcnt lgkmcnt(0)
	v_mul_f32_e32 v47, v57, v47
	v_mul_f32_e32 v42, v51, v45
	v_fmac_f32_e32 v47, v56, v46
	v_mul_f32_e32 v46, v55, v49
	v_fmac_f32_e32 v42, v50, v44
	v_fmac_f32_e32 v46, v54, v48
	v_add_f32_e32 v60, v43, v42
	v_add_f32_e32 v46, v47, v46
	v_add_f32_e32 v46, v60, v46
	ds_read_b128 v[42:45], v113
	v_add_f32_e32 v60, v151, v46
	ds_read_b128 v[46:49], v114
	s_waitcnt lgkmcnt(1)
	v_mul_f32_e32 v43, v53, v43
	v_fmac_f32_e32 v43, v52, v42
	s_waitcnt lgkmcnt(0)
	v_mul_f32_e32 v47, v57, v47
	v_mul_f32_e32 v42, v51, v45
	v_fmac_f32_e32 v47, v56, v46
	v_mul_f32_e32 v46, v55, v49
	v_fmac_f32_e32 v42, v50, v44
	v_fmac_f32_e32 v46, v54, v48
	v_add_f32_e32 v61, v43, v42
	v_add_f32_e32 v46, v47, v46
	v_add_f32_e32 v46, v61, v46
	ds_read_b128 v[42:45], v115
	v_add_f32_e32 v61, v152, v46
	ds_read_b128 v[46:49], v116
	s_waitcnt lgkmcnt(1)
	v_mul_f32_e32 v43, v53, v43
	v_fmac_f32_e32 v43, v52, v42
	s_waitcnt lgkmcnt(0)
	v_mul_f32_e32 v47, v57, v47
	v_mul_f32_e32 v42, v51, v45
	v_fmac_f32_e32 v47, v56, v46
	v_mul_f32_e32 v46, v55, v49
	v_fmac_f32_e32 v42, v50, v44
	v_fmac_f32_e32 v46, v54, v48
	v_add_f32_e32 v62, v43, v42
	v_add_f32_e32 v46, v47, v46
	v_add_f32_e32 v46, v62, v46
	ds_read_b128 v[42:45], v117
	v_add_f32_e32 v62, v154, v46
	ds_read_b128 v[46:49], v118
	s_waitcnt lgkmcnt(1)
	v_mul_f32_e32 v43, v53, v43
	v_fmac_f32_e32 v43, v52, v42
	s_waitcnt lgkmcnt(0)
	v_mul_f32_e32 v47, v57, v47
	v_mul_f32_e32 v42, v51, v45
	v_fmac_f32_e32 v47, v56, v46
	v_mul_f32_e32 v46, v55, v49
	v_fmac_f32_e32 v42, v50, v44
	v_fmac_f32_e32 v46, v54, v48
	v_add_f32_e32 v63, v43, v42
	v_add_f32_e32 v46, v47, v46
	v_add_f32_e32 v46, v63, v46
	ds_read_b128 v[42:45], v119
	v_add_f32_e32 v63, v156, v46
	ds_read_b128 v[46:49], v120
	s_waitcnt lgkmcnt(1)
	v_mul_f32_e32 v43, v53, v43
	v_fmac_f32_e32 v43, v52, v42
	s_waitcnt lgkmcnt(0)
	v_mul_f32_e32 v47, v57, v47
	v_mul_f32_e32 v42, v51, v45
	v_fmac_f32_e32 v47, v56, v46
	v_mul_f32_e32 v46, v55, v49
	v_fmac_f32_e32 v42, v50, v44
	v_fmac_f32_e32 v46, v54, v48
	v_add_f32_e32 v64, v43, v42
	v_add_f32_e32 v46, v47, v46
	ds_read_b128 v[42:45], v121
	v_add_f32_e32 v46, v64, v46
	v_add_f32_e32 v64, v153, v46
	ds_read_b128 v[46:49], v122
	s_waitcnt lgkmcnt(1)
	v_mul_f32_e32 v43, v53, v43
	v_fmac_f32_e32 v43, v52, v42
	v_mul_f32_e32 v42, v51, v45
	s_waitcnt lgkmcnt(0)
	v_mul_f32_e32 v47, v57, v47
	v_fmac_f32_e32 v42, v50, v44
	v_fmac_f32_e32 v47, v56, v46
	v_mul_f32_e32 v46, v55, v49
	v_add_f32_e32 v65, v43, v42
	v_fmac_f32_e32 v46, v54, v48
	ds_read_b128 v[42:45], v123
	v_add_f32_e32 v46, v47, v46
	v_add_f32_e32 v46, v65, v46
	v_add_f32_e32 v65, v155, v46
	ds_read_b128 v[46:49], v124
	s_waitcnt lgkmcnt(1)
	v_mul_f32_e32 v43, v53, v43
	v_fmac_f32_e32 v43, v52, v42
	v_mul_f32_e32 v42, v51, v45
	v_fmac_f32_e32 v42, v50, v44
	v_add_f32_e32 v42, v43, v42
	s_waitcnt lgkmcnt(0)
	v_mul_f32_e32 v43, v57, v47
	v_mul_f32_e32 v44, v55, v49
	v_fmac_f32_e32 v43, v56, v46
	v_fmac_f32_e32 v44, v54, v48
	v_add_f32_e32 v43, v43, v44
	v_add_f32_e32 v42, v42, v43
	v_add_f32_e32 v52, v58, v42
	v_pk_mul_f32 v[42:43], v[76:77], v[38:39] op_sel_hi:[0,1]
	v_pk_mul_f32 v[50:51], v[42:43], v[26:27]
	ds_read_b128 v[42:45], v125
	ds_read_b128 v[46:49], v126
	v_pk_mul_f32 v[38:39], v[76:77], v[40:41] op_sel_hi:[0,1]
	v_pk_mul_f32 v[40:41], v[36:37], v[32:33]
	v_pk_mul_f32 v[36:37], v[34:35], v[30:31]
	v_pk_mul_f32 v[38:39], v[38:39], v[28:29]
	s_waitcnt lgkmcnt(1)
	v_mul_f32_e32 v35, v51, v43
	s_waitcnt lgkmcnt(0)
	v_mul_f32_e32 v47, v37, v47
	v_fmac_f32_e32 v35, v50, v42
	v_mul_f32_e32 v42, v39, v45
	v_fmac_f32_e32 v47, v36, v46
	v_mul_f32_e32 v46, v41, v49
	v_fmac_f32_e32 v42, v38, v44
	v_fmac_f32_e32 v46, v40, v48
	v_add_f32_e32 v35, v35, v42
	v_add_f32_e32 v46, v47, v46
	ds_read_b128 v[42:45], v127
	v_add_f32_e32 v35, v35, v46
	ds_read_b128 v[46:49], v128
	v_add_f32_e32 v35, v59, v35
	v_cvt_pk_bf16_f32 v34, v50, v51
	s_waitcnt lgkmcnt(1)
	v_mul_f32_e32 v43, v51, v43
	v_fmac_f32_e32 v43, v50, v42
	s_waitcnt lgkmcnt(0)
	v_mul_f32_e32 v47, v37, v47
	v_mul_f32_e32 v42, v39, v45
	v_fmac_f32_e32 v47, v36, v46
	v_mul_f32_e32 v46, v41, v49
	v_fmac_f32_e32 v42, v38, v44
	v_fmac_f32_e32 v46, v40, v48
	v_add_f32_e32 v53, v43, v42
	v_add_f32_e32 v46, v47, v46
	v_add_f32_e32 v46, v53, v46
	ds_read_b128 v[42:45], v129
	v_add_f32_e32 v53, v60, v46
	ds_read_b128 v[46:49], v130
	s_waitcnt lgkmcnt(1)
	v_mul_f32_e32 v43, v51, v43
	v_fmac_f32_e32 v43, v50, v42
	s_waitcnt lgkmcnt(0)
	v_mul_f32_e32 v47, v37, v47
	v_mul_f32_e32 v42, v39, v45
	v_fmac_f32_e32 v47, v36, v46
	v_mul_f32_e32 v46, v41, v49
	v_fmac_f32_e32 v42, v38, v44
	v_fmac_f32_e32 v46, v40, v48
	v_add_f32_e32 v54, v43, v42
	v_add_f32_e32 v46, v47, v46
	v_add_f32_e32 v46, v54, v46
	ds_read_b128 v[42:45], v131
	v_add_f32_e32 v54, v61, v46
	ds_read_b128 v[46:49], v132
	s_waitcnt lgkmcnt(1)
	v_mul_f32_e32 v43, v51, v43
	v_fmac_f32_e32 v43, v50, v42
	s_waitcnt lgkmcnt(0)
	v_mul_f32_e32 v47, v37, v47
	v_mul_f32_e32 v42, v39, v45
	v_fmac_f32_e32 v47, v36, v46
	v_mul_f32_e32 v46, v41, v49
	v_fmac_f32_e32 v42, v38, v44
	v_fmac_f32_e32 v46, v40, v48
	v_add_f32_e32 v55, v43, v42
	v_add_f32_e32 v46, v47, v46
	v_add_f32_e32 v46, v55, v46
	ds_read_b128 v[42:45], v133
	v_add_f32_e32 v55, v62, v46
	ds_read_b128 v[46:49], v134
	s_waitcnt lgkmcnt(1)
	v_mul_f32_e32 v43, v51, v43
	v_fmac_f32_e32 v43, v50, v42
	s_waitcnt lgkmcnt(0)
	v_mul_f32_e32 v47, v37, v47
	v_mul_f32_e32 v42, v39, v45
	v_fmac_f32_e32 v47, v36, v46
	v_mul_f32_e32 v46, v41, v49
	v_fmac_f32_e32 v42, v38, v44
	v_fmac_f32_e32 v46, v40, v48
	v_add_f32_e32 v56, v43, v42
	v_add_f32_e32 v46, v47, v46
	ds_read_b128 v[42:45], v135
	v_add_f32_e32 v46, v56, v46
	v_add_f32_e32 v56, v63, v46
	ds_read_b128 v[46:49], v136
	s_waitcnt lgkmcnt(1)
	v_mul_f32_e32 v43, v51, v43
	v_fmac_f32_e32 v43, v50, v42
	v_mul_f32_e32 v42, v39, v45
	s_waitcnt lgkmcnt(0)
	v_mul_f32_e32 v47, v37, v47
	v_fmac_f32_e32 v42, v38, v44
	v_fmac_f32_e32 v47, v36, v46
	v_mul_f32_e32 v46, v41, v49
	v_add_f32_e32 v57, v43, v42
	v_fmac_f32_e32 v46, v40, v48
	ds_read_b128 v[42:45], v137
	v_add_f32_e32 v46, v47, v46
	v_add_f32_e32 v46, v57, v46
	v_add_f32_e32 v57, v64, v46
	ds_read_b128 v[46:49], v138
	s_waitcnt lgkmcnt(1)
	v_mul_f32_e32 v43, v51, v43
	v_fmac_f32_e32 v43, v50, v42
	v_mul_f32_e32 v42, v39, v45
	v_fmac_f32_e32 v42, v38, v44
	v_add_f32_e32 v58, v43, v42
	s_waitcnt lgkmcnt(0)
	v_mul_f32_e32 v47, v37, v47
	ds_read_b128 v[42:45], v139
	v_fmac_f32_e32 v47, v36, v46
	v_mul_f32_e32 v46, v41, v49
	v_fmac_f32_e32 v46, v40, v48
	v_add_f32_e32 v46, v47, v46
	v_add_f32_e32 v46, v58, v46
	v_add_f32_e32 v58, v65, v46
	ds_read_b128 v[46:49], v140
	s_waitcnt lgkmcnt(1)
	v_mul_f32_e32 v43, v51, v43
	v_fmac_f32_e32 v43, v50, v42
	ds_bpermute_b32 v42, v67, v35
	v_mul_f32_e32 v45, v39, v45
	v_fmac_f32_e32 v45, v38, v44
	v_add_f32_e32 v43, v43, v45
	ds_bpermute_b32 v45, v67, v53
	s_waitcnt lgkmcnt(1)
	v_add_f32_e32 v35, v35, v42
	ds_bpermute_b32 v42, v149, v35
	v_mul_f32_e32 v44, v37, v47
	v_fmac_f32_e32 v44, v36, v46
	s_waitcnt lgkmcnt(1)
	v_add_f32_e32 v45, v53, v45
	ds_bpermute_b32 v47, v149, v45
	s_waitcnt lgkmcnt(1)
	v_add_f32_e32 v35, v35, v42
	ds_bpermute_b32 v42, v148, v35
	v_mul_f32_e32 v46, v41, v49
	v_fmac_f32_e32 v46, v40, v48
	v_add_f32_e32 v44, v44, v46
	v_add_f32_e32 v43, v43, v44
	s_waitcnt lgkmcnt(0)
	v_add_f32_e32 v35, v35, v42
	v_add_f32_e32 v44, v45, v47
	ds_bpermute_b32 v42, v147, v35
	ds_bpermute_b32 v45, v148, v44
	v_add_f32_e32 v52, v52, v43
	ds_bpermute_b32 v43, v67, v54
	ds_bpermute_b32 v53, v67, v57
	s_waitcnt lgkmcnt(3)
	v_add_f32_e32 v35, v35, v42
	s_waitcnt lgkmcnt(2)
	v_add_f32_e32 v44, v44, v45
	ds_bpermute_b32 v42, v146, v35
	s_waitcnt lgkmcnt(2)
	v_add_f32_e32 v46, v54, v43
	ds_bpermute_b32 v45, v147, v44
	ds_bpermute_b32 v47, v149, v46
	ds_bpermute_b32 v54, v67, v52
	s_waitcnt lgkmcnt(3)
	v_add_f32_e32 v42, v35, v42
	v_add_f32_e32 v53, v57, v53
	s_waitcnt lgkmcnt(2)
	v_add_f32_e32 v35, v44, v45
	s_waitcnt lgkmcnt(1)
	v_add_f32_e32 v45, v46, v47
	ds_bpermute_b32 v44, v67, v55
	ds_bpermute_b32 v46, v148, v45
	ds_bpermute_b32 v47, v67, v56
	ds_bpermute_b32 v48, v146, v35
	s_waitcnt lgkmcnt(4)
	v_add_f32_e32 v52, v52, v54
	s_waitcnt lgkmcnt(3)
	v_add_f32_e32 v44, v55, v44
	s_waitcnt lgkmcnt(2)
	v_add_f32_e32 v45, v45, v46
	s_waitcnt lgkmcnt(1)
	v_add_f32_e32 v46, v56, v47
	ds_bpermute_b32 v49, v149, v44
	ds_bpermute_b32 v47, v149, v46
	ds_bpermute_b32 v50, v147, v45
	ds_bpermute_b32 v55, v149, v53
	ds_bpermute_b32 v54, v149, v52
	s_waitcnt lgkmcnt(4)
	v_add_f32_e32 v49, v44, v49
	v_add_f32_e32 v44, v35, v48
	s_waitcnt lgkmcnt(3)
	v_add_f32_e32 v35, v46, v47
	ds_bpermute_b32 v46, v148, v35
	ds_bpermute_b32 v51, v148, v49
	s_waitcnt lgkmcnt(4)
	v_add_f32_e32 v47, v45, v50
	ds_bpermute_b32 v50, v146, v47
	s_waitcnt lgkmcnt(4)
	v_add_f32_e32 v53, v53, v55
	s_waitcnt lgkmcnt(2)
	v_add_f32_e32 v35, v35, v46
	s_waitcnt lgkmcnt(1)
	v_add_f32_e32 v48, v49, v51
	ds_bpermute_b32 v51, v147, v35
	s_waitcnt lgkmcnt(1)
	v_add_f32_e32 v46, v47, v50
	v_add_f32_e32 v52, v52, v54
	ds_bpermute_b32 v55, v148, v53
	ds_bpermute_b32 v54, v148, v52
	s_waitcnt lgkmcnt(2)
	v_add_f32_e32 v35, v35, v51
	ds_bpermute_b32 v50, v146, v35
	ds_bpermute_b32 v49, v147, v48
	s_waitcnt lgkmcnt(3)
	v_add_f32_e32 v53, v53, v55
	s_waitcnt lgkmcnt(2)
	v_add_f32_e32 v52, v52, v54
	ds_bpermute_b32 v55, v147, v53
	s_waitcnt lgkmcnt(2)
	v_add_f32_e32 v50, v35, v50
	ds_bpermute_b32 v35, v67, v58
	ds_bpermute_b32 v54, v147, v52
	s_waitcnt lgkmcnt(3)
	v_add_f32_e32 v48, v48, v49
	s_waitcnt lgkmcnt(2)
	v_add_f32_e32 v53, v53, v55
	ds_bpermute_b32 v49, v146, v48
	s_waitcnt lgkmcnt(2)
	v_add_f32_e32 v35, v58, v35
	ds_bpermute_b32 v56, v149, v35
	s_waitcnt lgkmcnt(2)
	v_add_f32_e32 v57, v52, v54
	ds_bpermute_b32 v55, v146, v53
	ds_bpermute_b32 v58, v146, v57
	s_waitcnt lgkmcnt(3)
	v_add_f32_e32 v48, v48, v49
	s_waitcnt lgkmcnt(2)
	v_add_f32_e32 v35, v35, v56
	ds_bpermute_b32 v56, v148, v35
	s_waitcnt lgkmcnt(2)
	v_add_f32_e32 v52, v53, v55
	ds_bpermute_b32 v43, v75, v42
	ds_bpermute_b32 v45, v75, v44
	ds_bpermute_b32 v47, v75, v46
	s_waitcnt lgkmcnt(3)
	v_add_f32_e32 v35, v35, v56
	ds_bpermute_b32 v56, v147, v35
	ds_bpermute_b32 v49, v75, v48
	ds_bpermute_b32 v51, v75, v50
	ds_bpermute_b32 v53, v75, v52
	v_cvt_pk_bf16_f32 v36, v36, v37
	s_waitcnt lgkmcnt(3)
	v_add_f32_e32 v35, v35, v56
	ds_bpermute_b32 v56, v146, v35
	v_cvt_pk_bf16_f32 v37, v40, v41
	s_waitcnt lgkmcnt(0)
	v_add_f32_e32 v54, v35, v56
	v_add_f32_e32 v56, v57, v58
	ds_bpermute_b32 v55, v75, v54
	ds_bpermute_b32 v57, v75, v56
	v_cvt_pk_bf16_f32 v35, v38, v39
	global_store_dwordx4 v[68:69], v[34:37], off
	s_and_saveexec_b64 s[16:17], s[0:1]
	s_cbranch_execz .LBB0_24
	v_add_f32_e32 v34, v44, v45
	v_add_f32_e32 v42, v42, v43
	v_add_f32_e32 v35, v46, v47
	v_cndmask_b32_e64 v42, v42, v34, s[2:3]
	v_add_f32_e32 v41, v48, v49
	v_cndmask_b32_e64 v42, v42, v35, s[4:5]
	v_add_f32_e32 v40, v50, v51
	v_cndmask_b32_e64 v41, v42, v41, s[6:7]
	v_add_f32_e32 v39, v52, v53
	v_cndmask_b32_e64 v40, v41, v40, s[8:9]
	s_waitcnt lgkmcnt(1)
	v_add_f32_e32 v38, v54, v55
	v_cndmask_b32_e64 v39, v40, v39, s[10:11]
	s_waitcnt lgkmcnt(0)
	v_add_f32_e32 v37, v56, v57
	v_cndmask_b32_e64 v38, v39, v38, s[12:13]
	v_cndmask_b32_e64 v37, v38, v37, s[14:15]
	s_ashr_i32 s20, s40, 9
	v_and_or_b32 v34, s20, -8, v1
	v_ashrrev_i32_e32 v35, 31, v34
	s_and_b32 s41, s40, 0xfff
	v_lshlrev_b64 v[34:35], 14, v[34:35]
	s_lshl_b32 s20, s41, 2
	v_lshl_add_u64 v[34:35], s[22:23], 0, v[34:35]
	v_lshl_add_u64 v[34:35], v[34:35], 0, s[20:21]
	v_add_f32_e32 v36, v37, v178
	v_mul_f32_e64 v37, |v36|, s31
	v_fma_f32 v38, |v36|, s31, -v37
	v_rndne_f32_e32 v39, v37
	v_fma_f32 v38, |v36|, s33, v38
	v_sub_f32_e32 v37, v37, v39
	v_add_f32_e32 v37, v37, v38
	v_cvt_i32_f32_e32 v39, v39
	v_exp_f32_e32 v37, v37
	v_cmp_ngt_f32_e64 vcc, |v36|, s34
	v_min_f32_e32 v50, 0, v36
	v_ldexp_f32 v37, v37, v39
	v_cndmask_b32_e32 v37, 0, v37, vcc
	v_cmp_nlt_f32_e64 vcc, |v36|, s35
	s_nop 1
	v_cndmask_b32_e32 v51, v145, v37, vcc
	v_add_f32_e32 v38, 1.0, v51
	v_add_f32_e32 v39, -1.0, v38
	v_frexp_mant_f32_e32 v40, v38
	v_cvt_f64_f32_e32 v[36:37], v38
	v_sub_f32_e32 v41, v39, v38
	v_frexp_exp_i32_f64_e32 v36, v[36:37]
	v_cmp_gt_f32_e32 vcc, s37, v40
	v_sub_f32_e32 v39, v51, v39
	v_add_f32_e32 v37, 1.0, v41
	v_subbrev_co_u32_e32 v36, vcc, 0, v36, vcc
	v_add_f32_e32 v37, v39, v37
	v_sub_u32_e32 v39, 0, v36
	v_ldexp_f32 v38, v38, v39
	v_add_f32_e32 v40, -1.0, v38
	v_add_f32_e32 v41, 1.0, v38
	v_ldexp_f32 v37, v37, v39
	v_add_f32_e32 v39, 1.0, v40
	v_add_f32_e32 v42, -1.0, v41
	v_sub_f32_e32 v39, v38, v39
	v_sub_f32_e32 v38, v38, v42
	v_add_f32_e32 v42, v37, v39
	v_add_f32_e32 v37, v37, v38
	v_add_f32_e32 v44, v41, v37
	v_rcp_f32_e32 v45, v44
	v_add_f32_e32 v39, v40, v42
	v_sub_f32_e32 v40, v40, v39
	v_sub_f32_e32 v38, v41, v44
	v_mul_f32_e32 v47, v39, v45
	v_add_f32_e32 v46, v42, v40
	v_mul_f32_e32 v40, v44, v47
	v_add_f32_e32 v37, v37, v38
	v_fma_f32 v42, v47, v44, -v40
	v_fmac_f32_e32 v42, v47, v37
	v_add_f32_e32 v38, v40, v42
	v_sub_f32_e32 v41, v39, v38
	v_mov_b32_e32 v43, v38
	v_pk_add_f32 v[38:39], v[38:39], v[40:41] neg_lo:[0,1] neg_hi:[0,1]
	v_cvt_f32_i32_e32 v36, v36
	v_pk_add_f32 v[38:39], v[38:39], v[42:43] neg_lo:[0,1] neg_hi:[0,1]
	v_cmp_neq_f32_e32 vcc, s36, v51
	v_add_f32_e32 v39, v46, v39
	v_add_f32_e32 v38, v38, v39
	v_add_f32_e32 v39, v41, v38
	v_mul_f32_e32 v43, v45, v39
	v_mul_f32_e32 v40, v44, v43
	v_sub_f32_e32 v41, v41, v39
	v_add_f32_e32 v48, v47, v43
	v_fma_f32 v42, v43, v44, -v40
	v_add_f32_e32 v46, v38, v41
	v_sub_f32_e32 v38, v48, v47
	v_fmac_f32_e32 v42, v43, v37
	v_sub_f32_e32 v37, v43, v38
	v_add_f32_e32 v38, v40, v42
	v_sub_f32_e32 v41, v39, v38
	v_mov_b32_e32 v43, v38
	v_pk_add_f32 v[38:39], v[38:39], v[40:41] neg_lo:[0,1] neg_hi:[0,1]
	s_nop 0
	v_pk_add_f32 v[38:39], v[38:39], v[42:43] neg_lo:[0,1] neg_hi:[0,1]
	s_nop 0
	v_add_f32_e32 v39, v46, v39
	v_add_f32_e32 v38, v38, v39
	v_add_f32_e32 v38, v41, v38
	v_mul_f32_e32 v38, v45, v38
	v_add_f32_e32 v37, v37, v38
	v_add_f32_e32 v38, v48, v37
	v_mul_f32_e32 v40, v38, v38
	v_sub_f32_e32 v41, v38, v48
	v_fmamk_f32 v42, v40, 0x3e9b6dac, v144
	v_sub_f32_e32 v41, v37, v41
	v_mul_f32_e32 v37, v38, v40
	v_fmaak_f32 v75, v40, v42, 0x3f2aaada
	v_ldexp_f32 v43, v41, 1
	v_pk_mul_f32 v[40:41], v[36:37], v[74:75]
	v_ldexp_f32 v39, v38, 1
	v_fma_f32 v38, v36, s38, -v40
	v_fmac_f32_e32 v38, 0xb102e308, v36
	v_pk_add_f32 v[36:37], v[40:41], v[38:39]
	v_mov_b32_e32 v42, v40
	v_sub_f32_e32 v46, v37, v39
	v_pk_add_f32 v[44:45], v[36:37], v[40:41] neg_lo:[0,1] neg_hi:[0,1]
	v_sub_f32_e32 v40, v41, v46
	v_add_f32_e32 v43, v43, v40
	v_pk_add_f32 v[40:41], v[36:37], v[42:43]
	v_mov_b32_e32 v39, v36
	v_mov_b32_e32 v45, v41
	v_pk_add_f32 v[48:49], v[38:39], v[44:45] neg_lo:[0,1] neg_hi:[0,1]
	v_pk_add_f32 v[38:39], v[38:39], v[44:45]
	v_mov_b32_e32 v47, v36
	v_pk_add_f32 v[44:45], v[38:39], v[36:37] op_sel:[1,0] op_sel_hi:[0,1] neg_lo:[0,1] neg_hi:[0,1]
	v_mov_b32_e32 v46, v43
	v_mov_b32_e32 v42, v41
	v_mov_b32_e32 v43, v39
	v_pk_mov_b32 v[36:37], v[36:37], v[44:45] op_sel:[1,0]
	v_pk_add_f32 v[40:41], v[40:41], v[44:45] op_sel_hi:[1,0] neg_lo:[0,1] neg_hi:[0,1]
	v_pk_add_f32 v[36:37], v[42:43], v[36:37] neg_lo:[0,1] neg_hi:[0,1]
	v_mov_b32_e32 v40, v48
	v_pk_add_f32 v[36:37], v[46:47], v[36:37] neg_lo:[0,1] neg_hi:[0,1]
	v_mov_b32_e32 v49, v39
	v_pk_add_f32 v[40:41], v[40:41], v[36:37]
	s_nop 0
	v_pk_add_f32 v[42:43], v[40:41], v[40:41] op_sel:[0,1] op_sel_hi:[1,0]
	s_nop 0
	v_pk_add_f32 v[38:39], v[38:39], v[42:43] op_sel:[1,0] op_sel_hi:[0,1]
	v_mov_b32_e32 v41, v38
	v_mov_b32_e32 v37, v42
	v_pk_add_f32 v[42:43], v[40:41], v[48:49] neg_lo:[0,1] neg_hi:[0,1]
	s_nop 0
	v_sub_f32_e32 v39, v40, v42
	v_pk_add_f32 v[36:37], v[36:37], v[42:43] neg_lo:[0,1] neg_hi:[0,1]
	v_sub_f32_e32 v39, v48, v39
	v_add_f32_e32 v36, v36, v39
	v_add_f32_e32 v36, v36, v37
	v_add_f32_e32 v36, v38, v36
	v_cndmask_b32_e32 v36, v145, v36, vcc
	v_cmp_lt_f32_e64 vcc, |v51|, s39
	s_nop 1
	v_cndmask_b32_e32 v36, v36, v51, vcc
	v_sub_f32_e32 v36, v50, v36
	v_mov_b32_e32 v216, v34
	v_mov_b32_e32 v217, v35
	v_mov_b32_e32 v218, v36
	s_branch .LBB0_24
.Lp0_fin:
	s_and_saveexec_b64 s[16:17], s[0:1]
	global_store_dword v[216:217], v218, off
	s_or_b64 exec, exec, s[16:17]
	s_branch .LBB0_27
